# v042 + non-temporal hint on the P7 (layer 0 down GEMM) A-operand LDS-DMA loads
# baseline (speedup 1.0000x reference)
.LBB0_587:
	ds_read_b128 v[18:21], v193
	ds_read_b128 v[22:25], v194
	ds_read_b128 v[26:29], v195
	ds_read_b128 v[30:33], v196
	ds_read_b128 v[2:5], v197
	ds_read_b128 v[6:9], v198
	ds_read_b128 v[10:13], v199
	ds_read_b128 v[14:17], v200
	s_add_u32 s36, s22, 0x80
	s_addc_u32 s37, s23, 0
	s_cmp_eq_u32 s57, 4
	s_cselect_b32 s37, s11, s37
	s_cselect_b32 s36, s41, s36
	s_cselect_b32 s43, s1, s19
	s_cselect_b32 s42, s13, s18
	v_lshl_add_u64 v[188:189], s[22:23], 0, v[176:177]
	s_add_i32 m0, s29, 0xc000
	ds_read_b128 v[180:183], v210
	ds_read_b128 v[184:187], v210 offset:1024
	ds_read_b128 v[220:223], v210 offset:2048
	ds_read_b128 v[224:227], v210 offset:3072
	ds_read_b128 v[228:231], v210 offset:4096
	ds_read_b128 v[232:235], v210 offset:5120
	ds_read_b128 v[236:239], v210 offset:6144
	ds_read_b128 v[240:243], v210 offset:7168
	global_load_lds_dwordx4 v[188:189], off nt
	v_lshl_add_u64 v[188:189], s[22:23], 0, v[178:179]
	s_add_i32 m0, s29, 0xe000
	s_nop 0
	global_load_lds_dwordx4 v[188:189], off nt
	s_waitcnt vmcnt(8)
	s_waitcnt lgkmcnt(0)
	s_barrier
	s_setprio 1
	s_waitcnt lgkmcnt(0)
	v_mfma_scale_f32_16x16x128_f8f6f4 v[158:161], v[18:25], v[180:187], v[158:161], v211, v211 op_sel_hi:[0,0,0]
	v_mfma_scale_f32_16x16x128_f8f6f4 v[154:157], v[26:33], v[180:187], v[154:157], v211, v211 op_sel_hi:[0,0,0]
	v_mfma_scale_f32_16x16x128_f8f6f4 v[150:153], v[18:25], v[220:227], v[150:153], v211, v211 op_sel_hi:[0,0,0]
	v_mfma_scale_f32_16x16x128_f8f6f4 v[146:149], v[26:33], v[220:227], v[146:149], v211, v211 op_sel_hi:[0,0,0]
	v_mfma_scale_f32_16x16x128_f8f6f4 v[142:145], v[18:25], v[228:235], v[142:145], v211, v211 op_sel_hi:[0,0,0]
	v_mfma_scale_f32_16x16x128_f8f6f4 v[138:141], v[26:33], v[228:235], v[138:141], v211, v211 op_sel_hi:[0,0,0]
	v_mfma_scale_f32_16x16x128_f8f6f4 v[134:137], v[18:25], v[236:243], v[134:137], v211, v211 op_sel_hi:[0,0,0]
	v_mfma_scale_f32_16x16x128_f8f6f4 v[130:133], v[26:33], v[236:243], v[130:133], v211, v211 op_sel_hi:[0,0,0]
	s_setprio 0
	s_setprio 1
	v_mfma_scale_f32_16x16x128_f8f6f4 v[94:97], v[2:9], v[180:187], v[94:97], v211, v211 op_sel_hi:[0,0,0]
	v_mfma_scale_f32_16x16x128_f8f6f4 v[90:93], v[10:17], v[180:187], v[90:93], v211, v211 op_sel_hi:[0,0,0]
	v_mfma_scale_f32_16x16x128_f8f6f4 v[86:89], v[2:9], v[220:227], v[86:89], v211, v211 op_sel_hi:[0,0,0]
	v_mfma_scale_f32_16x16x128_f8f6f4 v[82:85], v[10:17], v[220:227], v[82:85], v211, v211 op_sel_hi:[0,0,0]
	v_mfma_scale_f32_16x16x128_f8f6f4 v[78:81], v[2:9], v[228:235], v[78:81], v211, v211 op_sel_hi:[0,0,0]
	v_mfma_scale_f32_16x16x128_f8f6f4 v[74:77], v[10:17], v[228:235], v[74:77], v211, v211 op_sel_hi:[0,0,0]
	v_mfma_scale_f32_16x16x128_f8f6f4 v[62:65], v[2:9], v[236:243], v[62:65], v211, v211 op_sel_hi:[0,0,0]
	v_mfma_scale_f32_16x16x128_f8f6f4 v[58:61], v[10:17], v[236:243], v[58:61], v211, v211 op_sel_hi:[0,0,0]
	s_setprio 0
	s_barrier
	s_mov_b32 m0, s31
	v_lshl_add_u64 v[180:181], s[42:43], 0, v[162:163]
	s_add_u32 s62, s42, 0x20000
	ds_read_b128 v[220:223], v210 offset:16384
	ds_read_b128 v[224:227], v210 offset:17408
	ds_read_b128 v[228:231], v210 offset:18432
	ds_read_b128 v[232:235], v210 offset:19456
	ds_read_b128 v[236:239], v210 offset:20480
	ds_read_b128 v[240:243], v210 offset:21504
	ds_read_b128 v[244:247], v210 offset:22528
	ds_read_b128 v[248:251], v210 offset:23552
	global_load_lds_dwordx4 v[180:181], off
	v_lshl_add_u64 v[182:183], s[42:43], 0, v[164:165]
	s_mov_b32 m0, s34
	s_addc_u32 s63, s43, 0
	global_load_lds_dwordx4 v[182:183], off
	v_lshl_add_u64 v[184:185], s[62:63], 0, v[162:163]
	s_mov_b32 m0, s35
	v_lshl_add_u64 v[186:187], s[36:37], 0, v[170:171]
	global_load_lds_dwordx4 v[184:185], off
	v_lshl_add_u64 v[184:185], s[62:63], 0, v[164:165]
	s_mov_b32 m0, s44
	s_nop 0
	global_load_lds_dwordx4 v[184:185], off
	v_lshl_add_u64 v[184:185], s[36:37], 0, v[166:167]
	s_mov_b32 m0, s29
	s_nop 0
	global_load_lds_dwordx4 v[184:185], off nt
	s_mov_b32 m0, s45
	s_nop 0
	global_load_lds_dwordx4 v[186:187], off nt
	s_waitcnt vmcnt(8)
	s_waitcnt lgkmcnt(0)
	s_barrier
	s_setprio 1
	s_waitcnt lgkmcnt(0)
	v_mfma_scale_f32_16x16x128_f8f6f4 v[126:129], v[18:25], v[220:227], v[126:129], v211, v211 op_sel_hi:[0,0,0]
	v_mfma_scale_f32_16x16x128_f8f6f4 v[122:125], v[26:33], v[220:227], v[122:125], v211, v211 op_sel_hi:[0,0,0]
	v_mfma_scale_f32_16x16x128_f8f6f4 v[118:121], v[18:25], v[228:235], v[118:121], v211, v211 op_sel_hi:[0,0,0]
	v_mfma_scale_f32_16x16x128_f8f6f4 v[114:117], v[26:33], v[228:235], v[114:117], v211, v211 op_sel_hi:[0,0,0]
	v_mfma_scale_f32_16x16x128_f8f6f4 v[110:113], v[18:25], v[236:243], v[110:113], v211, v211 op_sel_hi:[0,0,0]
	v_mfma_scale_f32_16x16x128_f8f6f4 v[106:109], v[26:33], v[236:243], v[106:109], v211, v211 op_sel_hi:[0,0,0]
	v_mfma_scale_f32_16x16x128_f8f6f4 v[102:105], v[18:25], v[244:251], v[102:105], v211, v211 op_sel_hi:[0,0,0]
	v_mfma_scale_f32_16x16x128_f8f6f4 v[98:101], v[26:33], v[244:251], v[98:101], v211, v211 op_sel_hi:[0,0,0]
	s_setprio 0
	s_setprio 1
	v_mfma_scale_f32_16x16x128_f8f6f4 v[70:73], v[2:9], v[220:227], v[70:73], v211, v211 op_sel_hi:[0,0,0]
	v_mfma_scale_f32_16x16x128_f8f6f4 v[66:69], v[10:17], v[220:227], v[66:69], v211, v211 op_sel_hi:[0,0,0]
	v_mfma_scale_f32_16x16x128_f8f6f4 v[54:57], v[2:9], v[228:235], v[54:57], v211, v211 op_sel_hi:[0,0,0]
	v_mfma_scale_f32_16x16x128_f8f6f4 v[50:53], v[10:17], v[228:235], v[50:53], v211, v211 op_sel_hi:[0,0,0]
	v_mfma_scale_f32_16x16x128_f8f6f4 v[46:49], v[2:9], v[236:243], v[46:49], v211, v211 op_sel_hi:[0,0,0]
	v_mfma_scale_f32_16x16x128_f8f6f4 v[42:45], v[10:17], v[236:243], v[42:45], v211, v211 op_sel_hi:[0,0,0]
	v_mfma_scale_f32_16x16x128_f8f6f4 v[38:41], v[2:9], v[244:251], v[38:41], v211, v211 op_sel_hi:[0,0,0]
	v_mfma_scale_f32_16x16x128_f8f6f4 v[34:37], v[10:17], v[244:251], v[34:37], v211, v211 op_sel_hi:[0,0,0]
	s_setprio 0
	s_barrier
	ds_read_b128 v[2:5], v201
	ds_read_b128 v[6:9], v202
	ds_read_b128 v[10:13], v203
	ds_read_b128 v[14:17], v204
	ds_read_b128 v[18:21], v205
	ds_read_b128 v[22:25], v206
	ds_read_b128 v[26:29], v207
	ds_read_b128 v[30:33], v208
	s_mov_b32 m0, s46
	v_lshl_add_u64 v[188:189], s[36:37], 0, v[168:169]
	ds_read_b128 v[220:223], v210 offset:32768
	ds_read_b128 v[224:227], v210 offset:33792
	ds_read_b128 v[228:231], v210 offset:34816
	ds_read_b128 v[232:235], v210 offset:35840
	ds_read_b128 v[236:239], v210 offset:36864
	ds_read_b128 v[240:243], v210 offset:37888
	ds_read_b128 v[244:247], v210 offset:38912
	ds_read_b128 v[248:251], v210 offset:39936
	global_load_lds_dwordx4 v[188:189], off nt
	v_lshl_add_u64 v[188:189], s[36:37], 0, v[172:173]
	s_mov_b32 m0, s47
	s_nop 0
	global_load_lds_dwordx4 v[188:189], off nt
	s_waitcnt vmcnt(8)
	s_waitcnt lgkmcnt(0)
	s_barrier
	s_setprio 1
	s_waitcnt lgkmcnt(0)
	v_mfma_scale_f32_16x16x128_f8f6f4 v[158:161], v[2:9], v[220:227], v[158:161], v211, v211 op_sel_hi:[0,0,0]
	v_mfma_scale_f32_16x16x128_f8f6f4 v[154:157], v[10:17], v[220:227], v[154:157], v211, v211 op_sel_hi:[0,0,0]
	v_mfma_scale_f32_16x16x128_f8f6f4 v[150:153], v[2:9], v[228:235], v[150:153], v211, v211 op_sel_hi:[0,0,0]
	v_mfma_scale_f32_16x16x128_f8f6f4 v[146:149], v[10:17], v[228:235], v[146:149], v211, v211 op_sel_hi:[0,0,0]
	v_mfma_scale_f32_16x16x128_f8f6f4 v[142:145], v[2:9], v[236:243], v[142:145], v211, v211 op_sel_hi:[0,0,0]
	v_mfma_scale_f32_16x16x128_f8f6f4 v[138:141], v[10:17], v[236:243], v[138:141], v211, v211 op_sel_hi:[0,0,0]
	v_mfma_scale_f32_16x16x128_f8f6f4 v[134:137], v[2:9], v[244:251], v[134:137], v211, v211 op_sel_hi:[0,0,0]
	v_mfma_scale_f32_16x16x128_f8f6f4 v[130:133], v[10:17], v[244:251], v[130:133], v211, v211 op_sel_hi:[0,0,0]
	s_setprio 0
	s_setprio 1
	v_mfma_scale_f32_16x16x128_f8f6f4 v[94:97], v[18:25], v[220:227], v[94:97], v211, v211 op_sel_hi:[0,0,0]
	v_mfma_scale_f32_16x16x128_f8f6f4 v[90:93], v[26:33], v[220:227], v[90:93], v211, v211 op_sel_hi:[0,0,0]
	v_mfma_scale_f32_16x16x128_f8f6f4 v[86:89], v[18:25], v[228:235], v[86:89], v211, v211 op_sel_hi:[0,0,0]
	v_mfma_scale_f32_16x16x128_f8f6f4 v[82:85], v[26:33], v[228:235], v[82:85], v211, v211 op_sel_hi:[0,0,0]
	v_mfma_scale_f32_16x16x128_f8f6f4 v[78:81], v[18:25], v[236:243], v[78:81], v211, v211 op_sel_hi:[0,0,0]
	v_mfma_scale_f32_16x16x128_f8f6f4 v[74:77], v[26:33], v[236:243], v[74:77], v211, v211 op_sel_hi:[0,0,0]
	v_mfma_scale_f32_16x16x128_f8f6f4 v[62:65], v[18:25], v[244:251], v[62:65], v211, v211 op_sel_hi:[0,0,0]
	v_mfma_scale_f32_16x16x128_f8f6f4 v[58:61], v[26:33], v[244:251], v[58:61], v211, v211 op_sel_hi:[0,0,0]
	s_setprio 0
	s_barrier
	s_mov_b32 m0, s50
	v_lshl_add_u64 v[180:181], v[180:181], 0, s[4:5]
	s_add_u32 s36, s42, 0x20080
	ds_read_b128 v[220:223], v210 offset:49152
	ds_read_b128 v[224:227], v210 offset:50176
	ds_read_b128 v[228:231], v210 offset:51200
	ds_read_b128 v[232:235], v210 offset:52224
	ds_read_b128 v[236:239], v210 offset:53248
	ds_read_b128 v[240:243], v210 offset:54272
	ds_read_b128 v[244:247], v210 offset:55296
	ds_read_b128 v[248:251], v210 offset:56320
	global_load_lds_dwordx4 v[180:181], off
	v_lshl_add_u64 v[180:181], v[182:183], 0, s[4:5]
	s_mov_b32 m0, s51
	s_addc_u32 s37, s43, 0
	global_load_lds_dwordx4 v[180:181], off
	v_lshl_add_u64 v[180:181], s[36:37], 0, v[162:163]
	s_mov_b32 m0, s54
	s_nop 0
	global_load_lds_dwordx4 v[180:181], off
	v_lshl_add_u64 v[180:181], s[36:37], 0, v[164:165]
	s_mov_b32 m0, s55
	s_nop 0
	global_load_lds_dwordx4 v[180:181], off
	v_lshl_add_u64 v[180:181], v[184:185], 0, s[4:5]
	s_mov_b32 m0, s52
	s_nop 0
	global_load_lds_dwordx4 v[180:181], off nt
	v_lshl_add_u64 v[180:181], v[186:187], 0, s[4:5]
	s_mov_b32 m0, s53
	s_nop 0
	global_load_lds_dwordx4 v[180:181], off nt
	s_waitcnt vmcnt(8)
	s_waitcnt lgkmcnt(0)
	s_barrier
	s_setprio 1
	s_waitcnt lgkmcnt(0)
	v_mfma_scale_f32_16x16x128_f8f6f4 v[126:129], v[2:9], v[220:227], v[126:129], v211, v211 op_sel_hi:[0,0,0]
	v_mfma_scale_f32_16x16x128_f8f6f4 v[122:125], v[10:17], v[220:227], v[122:125], v211, v211 op_sel_hi:[0,0,0]
	v_mfma_scale_f32_16x16x128_f8f6f4 v[118:121], v[2:9], v[228:235], v[118:121], v211, v211 op_sel_hi:[0,0,0]
	v_mfma_scale_f32_16x16x128_f8f6f4 v[114:117], v[10:17], v[228:235], v[114:117], v211, v211 op_sel_hi:[0,0,0]
	v_mfma_scale_f32_16x16x128_f8f6f4 v[110:113], v[2:9], v[236:243], v[110:113], v211, v211 op_sel_hi:[0,0,0]
	v_mfma_scale_f32_16x16x128_f8f6f4 v[106:109], v[10:17], v[236:243], v[106:109], v211, v211 op_sel_hi:[0,0,0]
	v_mfma_scale_f32_16x16x128_f8f6f4 v[102:105], v[2:9], v[244:251], v[102:105], v211, v211 op_sel_hi:[0,0,0]
	v_mfma_scale_f32_16x16x128_f8f6f4 v[98:101], v[10:17], v[244:251], v[98:101], v211, v211 op_sel_hi:[0,0,0]
	s_setprio 0
	s_setprio 1
	v_mfma_scale_f32_16x16x128_f8f6f4 v[70:73], v[18:25], v[220:227], v[70:73], v211, v211 op_sel_hi:[0,0,0]
	v_mfma_scale_f32_16x16x128_f8f6f4 v[66:69], v[26:33], v[220:227], v[66:69], v211, v211 op_sel_hi:[0,0,0]
	v_mfma_scale_f32_16x16x128_f8f6f4 v[54:57], v[18:25], v[228:235], v[54:57], v211, v211 op_sel_hi:[0,0,0]
	v_mfma_scale_f32_16x16x128_f8f6f4 v[50:53], v[26:33], v[228:235], v[50:53], v211, v211 op_sel_hi:[0,0,0]
	v_mfma_scale_f32_16x16x128_f8f6f4 v[46:49], v[18:25], v[236:243], v[46:49], v211, v211 op_sel_hi:[0,0,0]
	v_mfma_scale_f32_16x16x128_f8f6f4 v[42:45], v[26:33], v[236:243], v[42:45], v211, v211 op_sel_hi:[0,0,0]
	v_mfma_scale_f32_16x16x128_f8f6f4 v[38:41], v[18:25], v[244:251], v[38:41], v211, v211 op_sel_hi:[0,0,0]
	v_mfma_scale_f32_16x16x128_f8f6f4 v[34:37], v[26:33], v[244:251], v[34:37], v211, v211 op_sel_hi:[0,0,0]
	s_setprio 0
	s_barrier
	s_add_i32 s57, s57, 2
	s_add_u32 s22, s22, 0x100
	s_addc_u32 s23, s23, 0
	s_add_u32 s18, s18, 0x100
	s_addc_u32 s19, s19, 0
	s_cmp_gt_u32 s57, 5
	s_cbranch_scc0 .LBB0_587
	s_and_b64 vcc, exec, s[6:7]
	s_cbranch_vccz .LBB0_590
	s_barrier
